# MLA QK: K fragment LDS reads run 4 ahead through an 8-quad ring with counted lgkmcnt instead of lgkmcnt(0) in front of each MFMA pair
# baseline (speedup 1.0000x reference)
; template <bool MLA>
; __device__ __forceinline__ void attn_unit(char* lds, int h, int qb, const bf16_t* Qp, int ldq, const bf16_t* Kp, int ldk, const bf16_t* KRp, const bf16_t* Vp, int ldv,
;                                           unsigned char* Op, int ldo, const float* KMp, const float* rel_bias) {
;     ...
;             { const char* kn = lds + buf * SHM_KN; const char* kr = lds + buf * SHM_KR;
; #pragma unroll
;               for (int d0 = 0; d0 < 8; ++d0) { const char* ap = kn + kan[d0 & 3] + (d0 >> 2) * 128;
;                   const bf16x8 a0 = *(const bf16x8*)ap, a1 = *(const bf16x8*)(ap + 32 * 256);
;                   p0 = __builtin_amdgcn_mfma_f32_32x32x16_bf16(a0, qr[d0], p0, 0, 0, 0);
;                   p1 = __builtin_amdgcn_mfma_f32_32x32x16_bf16(a1, qr[d0], p1, 0, 0, 0); }
;               if constexpr (MLA) {
; #pragma unroll
;                   for (int d0 = 8; d0 < 12; ++d0) { const char* ap = kr + kar[d0 & 3];
;                       const bf16x8 a0 = *(const bf16x8*)ap, a1 = *(const bf16x8*)(ap + 32 * 128);
;                       p0 = __builtin_amdgcn_mfma_f32_32x32x16_bf16(a0, qr[d0], p0, 0, 0, 0);
;                       p1 = __builtin_amdgcn_mfma_f32_32x32x16_bf16(a1, qr[d0], p1, 0, 0, 0); } } }
.LBB0_1388:
	s_sub_i32 s22, s10, 64
	s_cmp_le_u32 s22, s51
	s_cselect_b64 s[54:55], -1, 0
	v_cndmask_b32_e64 v66, 0, 1, s[54:55]
	s_nop 0
	v_readfirstlane_b32 s22, v66
	s_bitcmp0_b32 s22, 0
	s_cbranch_scc1 .Lmla_inact
	s_lshl_b32 s53, s46, 14
	s_lshl_b32 s23, s46, 13
	s_sub_i32 s22, s53, s23
	v_add3_u32 v234, s53, v154, v153
	v_add3_u32 v235, s53, v155, v153
	v_add3_u32 v236, s53, v156, v153
	v_add3_u32 v237, s53, v157, v153
	v_add3_u32 v238, s22, v154, v159
	v_add3_u32 v239, s22, v155, v159
	v_add3_u32 v240, s22, v156, v159
	v_add3_u32 v241, s22, v157, v159
	ds_read_b128 v[196:199], v234 offset:32768
	ds_read_b128 v[200:203], v234 offset:40960
	ds_read_b128 v[204:207], v235 offset:32768
	ds_read_b128 v[208:211], v235 offset:40960
	ds_read_b128 v[212:215], v236 offset:32768
	s_waitcnt lgkmcnt(4)
	v_mfma_f32_32x32x16_bf16 v[82:97], v[196:199], v[98:101], 0
	ds_read_b128 v[216:219], v236 offset:40960
	s_waitcnt lgkmcnt(4)
	v_mfma_f32_32x32x16_bf16 v[66:81], v[200:203], v[98:101], 0
	s_cmp_lt_u32 s52, s50
	s_cselect_b32 s101, 1, 0
	s_cbranch_scc0 .Lmla_nk0
	s_lshl_b64 s[98:99], s[10:11], 12
	s_add_u32 s98, s44, s98
	s_addc_u32 s99, s45, s99
	s_lshl_b32 s100, s46, 14
	s_xor_b32 s100, s100, 0x4000
	s_add_i32 s100, s48, s100
	s_add_i32 m0, s100, 0x8000
	v_lshl_add_u64 v[228:229], v[146:147], 1, s[98:99]
	global_load_lds_dwordx4 v176, s[98:99]
.Lmla_nk0:
	ds_read_b128 v[220:223], v237 offset:32768
	s_waitcnt lgkmcnt(4)
	v_mfma_f32_32x32x16_bf16 v[82:97], v[204:207], v[102:105], v[82:97]
	ds_read_b128 v[224:227], v237 offset:40960
	s_waitcnt lgkmcnt(4)
	v_mfma_f32_32x32x16_bf16 v[66:81], v[208:211], v[102:105], v[66:81]
	ds_read_b128 v[196:199], v234 offset:32896
	s_waitcnt lgkmcnt(4)
	v_mfma_f32_32x32x16_bf16 v[82:97], v[212:215], v[106:109], v[82:97]
	ds_read_b128 v[200:203], v234 offset:41088
	s_waitcnt lgkmcnt(4)
	v_mfma_f32_32x32x16_bf16 v[66:81], v[216:219], v[106:109], v[66:81]
	s_cmp_lg_u32 s101, 0
	s_cbranch_scc0 .Lmla_nk1
	v_lshl_add_u64 v[230:231], v[228:229], 0, s[38:39]
	s_mov_b32 m0, s100
	v_lshl_add_u64 v[228:229], v[228:229], 0, s[40:41]
	global_load_lds_dwordx4 v[230:231], off
.Lmla_nk1:
	ds_read_b128 v[204:207], v235 offset:32896
	s_waitcnt lgkmcnt(4)
	v_mfma_f32_32x32x16_bf16 v[82:97], v[220:223], v[110:113], v[82:97]
	ds_read_b128 v[208:211], v235 offset:41088
	s_waitcnt lgkmcnt(4)
	v_mfma_f32_32x32x16_bf16 v[66:81], v[224:227], v[110:113], v[66:81]
	ds_read_b128 v[212:215], v236 offset:32896
	s_waitcnt lgkmcnt(4)
	v_mfma_f32_32x32x16_bf16 v[82:97], v[196:199], v[114:117], v[82:97]
	ds_read_b128 v[216:219], v236 offset:41088
	s_waitcnt lgkmcnt(4)
	v_mfma_f32_32x32x16_bf16 v[66:81], v[200:203], v[114:117], v[66:81]
	s_cmp_lg_u32 s101, 0
	s_cbranch_scc0 .Lmla_nk2
	s_add_i32 m0, s100, 0x8400
	s_nop 0
	global_load_lds_dwordx4 v177, s[98:99]
.Lmla_nk2:
	ds_read_b128 v[220:223], v237 offset:32896
	s_waitcnt lgkmcnt(4)
	v_mfma_f32_32x32x16_bf16 v[82:97], v[204:207], v[118:121], v[82:97]
	ds_read_b128 v[224:227], v237 offset:41088
	s_waitcnt lgkmcnt(4)
	v_mfma_f32_32x32x16_bf16 v[66:81], v[208:211], v[118:121], v[66:81]
	ds_read_b128 v[196:199], v238
	s_waitcnt lgkmcnt(4)
	v_mfma_f32_32x32x16_bf16 v[82:97], v[212:215], v[122:125], v[82:97]
	ds_read_b128 v[200:203], v238 offset:4096
	s_waitcnt lgkmcnt(4)
	v_mfma_f32_32x32x16_bf16 v[66:81], v[216:219], v[122:125], v[66:81]
	s_cmp_lg_u32 s101, 0
	s_cbranch_scc0 .Lmla_nk3
	s_add_i32 m0, s100, 0x400
	s_nop 0
	global_load_lds_dwordx4 v[228:229], off
.Lmla_nk3:
	ds_read_b128 v[204:207], v239
	s_waitcnt lgkmcnt(4)
	v_mfma_f32_32x32x16_bf16 v[82:97], v[220:223], v[126:129], v[82:97]
	ds_read_b128 v[208:211], v239 offset:4096
	s_waitcnt lgkmcnt(4)
	v_mfma_f32_32x32x16_bf16 v[66:81], v[224:227], v[126:129], v[66:81]
	ds_read_b128 v[212:215], v240
	s_waitcnt lgkmcnt(4)
	v_mfma_f32_32x32x16_bf16 v[82:97], v[196:199], v[130:133], v[82:97]
	ds_read_b128 v[216:219], v240 offset:4096
	s_waitcnt lgkmcnt(4)
	v_mfma_f32_32x32x16_bf16 v[66:81], v[200:203], v[130:133], v[66:81]
	s_cmp_lg_u32 s101, 0
	s_cbranch_scc0 .Lmla_nk4
	s_lshl_b32 s100, s46, 13
	s_lshl_b64 s[98:99], s[10:11], 7
	s_xor_b32 s100, s100, 0x2000
	v_lshl_add_u64 v[228:229], v[148:149], 0, s[98:99]
	s_add_i32 m0, s49, s100
	s_nop 0
	global_load_lds_dwordx4 v[228:229], off
; template <bool MLA>
; __device__ __forceinline__ void attn_unit(char* lds, int h, int qb, const bf16_t* Qp, int ldq, const bf16_t* Kp, int ldk, const bf16_t* KRp, const bf16_t* Vp, int ldv,
;                                           unsigned char* Op, int ldo, const float* KMp, const float* rel_bias) {
;     ...
;               for (int d0 = 0; d0 < 8; ++d0) { const char* ap = kn + kan[d0 & 3] + (d0 >> 2) * 128;
;                   const bf16x8 a0 = *(const bf16x8*)ap, a1 = *(const bf16x8*)(ap + 32 * 256);
;                   p0 = __builtin_amdgcn_mfma_f32_32x32x16_bf16(a0, qr[d0], p0, 0, 0, 0);
;                   p1 = __builtin_amdgcn_mfma_f32_32x32x16_bf16(a1, qr[d0], p1, 0, 0, 0); }
;               if constexpr (MLA) {
; #pragma unroll
;                   for (int d0 = 8; d0 < 12; ++d0) { const char* ap = kr + kar[d0 & 3];
;                       const bf16x8 a0 = *(const bf16x8*)ap, a1 = *(const bf16x8*)(ap + 32 * 128);
;                       p0 = __builtin_amdgcn_mfma_f32_32x32x16_bf16(a0, qr[d0], p0, 0, 0, 0);
;                       p1 = __builtin_amdgcn_mfma_f32_32x32x16_bf16(a1, qr[d0], p1, 0, 0, 0); } } }
;             const int dq = qpos - kb - 4 * hi;
;             if constexpr (MLA) {
;                 if (kb + 63 > qlo) {
; #pragma unroll
;                     for (int r = 0; r < 16; ++r) { const int d0 = dq - CROWC(r); if (d0 < 0) p0[r] = NEG; if (d0 < 32) p1[r] = NEG; } }
.Lmla_nk4:
	ds_read_b128 v[220:223], v241
	s_waitcnt lgkmcnt(4)
	v_mfma_f32_32x32x16_bf16 v[82:97], v[204:207], v[134:137], v[82:97]
	ds_read_b128 v[224:227], v241 offset:4096
	s_waitcnt lgkmcnt(4)
	v_mfma_f32_32x32x16_bf16 v[66:81], v[208:211], v[134:137], v[66:81]
	s_waitcnt lgkmcnt(3)
	v_mfma_f32_32x32x16_bf16 v[82:97], v[212:215], v[138:141], v[82:97]
	s_waitcnt lgkmcnt(2)
	v_mfma_f32_32x32x16_bf16 v[66:81], v[216:219], v[138:141], v[66:81]
	s_waitcnt lgkmcnt(1)
	v_mfma_f32_32x32x16_bf16 v[82:97], v[220:223], v[142:145], v[82:97]
	s_waitcnt lgkmcnt(0)
	v_mfma_f32_32x32x16_bf16 v[66:81], v[224:227], v[142:145], v[66:81]
	s_add_i32 s22, s10, -1
	s_cmp_le_u32 s22, s42
	s_cbranch_scc1 .LBB0_1391
	v_add_u32_e32 v179, 27, v174
	v_cmp_lt_i32_e32 vcc, -1, v179
	s_nop 7
	v_cndmask_b32_e32 v82, v163, v82, vcc
	v_cmp_lt_i32_e32 vcc, 31, v179
	v_add_u32_e32 v179, 26, v174
	s_nop 0
	v_cndmask_b32_e32 v66, v163, v66, vcc
	v_cmp_lt_i32_e32 vcc, -1, v179
	s_nop 1
	v_cndmask_b32_e32 v83, v163, v83, vcc
	v_cmp_lt_i32_e32 vcc, 31, v179
	v_add_u32_e32 v179, 25, v174
	s_nop 0
	v_cndmask_b32_e32 v67, v163, v67, vcc
	v_cmp_lt_i32_e32 vcc, -1, v179
	s_nop 1
	v_cndmask_b32_e32 v84, v163, v84, vcc
	v_cmp_lt_i32_e32 vcc, 31, v179
	v_add_u32_e32 v179, 24, v174
	s_nop 0
	v_cndmask_b32_e32 v68, v163, v68, vcc
	v_cmp_lt_i32_e32 vcc, -1, v179
	s_nop 1
	v_cndmask_b32_e32 v85, v163, v85, vcc
	v_cmp_lt_i32_e32 vcc, 31, v179
	v_add_u32_e32 v179, 19, v174
	s_nop 0
	v_cndmask_b32_e32 v69, v163, v69, vcc
	v_cmp_lt_i32_e32 vcc, -1, v179
	s_nop 1
	v_cndmask_b32_e32 v86, v163, v86, vcc
	v_cmp_lt_i32_e32 vcc, 31, v179
	v_add_u32_e32 v179, 18, v174
	s_nop 0
	v_cndmask_b32_e32 v70, v163, v70, vcc
	v_cmp_lt_i32_e32 vcc, -1, v179
	s_nop 1
	v_cndmask_b32_e32 v87, v163, v87, vcc
	v_cmp_lt_i32_e32 vcc, 31, v179
	v_add_u32_e32 v179, 17, v174
	s_nop 0
	v_cndmask_b32_e32 v71, v163, v71, vcc
	v_cmp_lt_i32_e32 vcc, -1, v179
	s_nop 1
	v_cndmask_b32_e32 v88, v163, v88, vcc
	v_cmp_lt_i32_e32 vcc, 31, v179
	v_add_u32_e32 v179, 16, v174
	s_nop 0
	v_cndmask_b32_e32 v72, v163, v72, vcc
	v_cmp_lt_i32_e32 vcc, -1, v179
	s_nop 1
	v_cndmask_b32_e32 v89, v163, v89, vcc
	v_cmp_lt_i32_e32 vcc, 31, v179
	v_add_u32_e32 v179, 11, v174
	s_nop 0
	v_cndmask_b32_e32 v73, v163, v73, vcc
	v_cmp_lt_i32_e32 vcc, -1, v179
	s_nop 1
	v_cndmask_b32_e32 v90, v163, v90, vcc
	v_cmp_lt_i32_e32 vcc, 31, v179
	v_add_u32_e32 v179, 10, v174
	s_nop 0
	v_cndmask_b32_e32 v74, v163, v74, vcc
	v_cmp_lt_i32_e32 vcc, -1, v179
	s_nop 1
	v_cndmask_b32_e32 v91, v163, v91, vcc
	v_cmp_lt_i32_e32 vcc, 31, v179
	v_add_u32_e32 v179, 9, v174
	s_nop 0
	v_cndmask_b32_e32 v75, v163, v75, vcc
	v_cmp_lt_i32_e32 vcc, -1, v179
	s_nop 1
	v_cndmask_b32_e32 v92, v163, v92, vcc
	v_cmp_lt_i32_e32 vcc, 31, v179
	v_add_u32_e32 v179, 8, v174
	s_nop 0
	v_cndmask_b32_e32 v76, v163, v76, vcc
	v_cmp_lt_i32_e32 vcc, -1, v179
	s_nop 1
	v_cndmask_b32_e32 v93, v163, v93, vcc
	v_cmp_lt_i32_e32 vcc, 31, v179
	v_add_u32_e32 v179, 3, v174
	s_nop 0
	v_cndmask_b32_e32 v77, v163, v77, vcc
	v_cmp_lt_i32_e32 vcc, -1, v179
	s_nop 1
	v_cndmask_b32_e32 v94, v163, v94, vcc
	v_cmp_lt_i32_e32 vcc, 31, v179
	v_add_u32_e32 v179, 2, v174
	s_nop 0
	v_cndmask_b32_e32 v78, v163, v78, vcc
	v_cmp_lt_i32_e32 vcc, -1, v179
	s_nop 1
	v_cndmask_b32_e32 v95, v163, v95, vcc
	v_cmp_lt_i32_e32 vcc, 31, v179
	v_add_u32_e32 v179, 1, v174
	s_nop 0
	v_cndmask_b32_e32 v79, v163, v79, vcc
	v_cmp_lt_i32_e32 vcc, -1, v179
	s_nop 1
	v_cndmask_b32_e32 v96, v163, v96, vcc
	v_cmp_lt_i32_e32 vcc, 31, v179
	s_nop 1
	v_cndmask_b32_e32 v80, v163, v80, vcc
	v_cmp_lt_i32_e32 vcc, -1, v174
	s_nop 1
	v_cndmask_b32_e32 v97, v163, v97, vcc
	v_cmp_lt_i32_e32 vcc, 31, v174
	s_nop 1
	v_cndmask_b32_e32 v81, v163, v81, vcc
